# attention K ring swizzled by row&15 instead of row&7 (no 2-way bank conflict on the ds_read_b128 K fragment reads)
# baseline (speedup 1.0000x reference)
.LBB0_1016:
	s_add_u32 s28, s8, s6
	s_addc_u32 s29, s9, s7
	global_load_dwordx4 v[4:7], v1, s[28:29] offset:16
	global_load_dwordx4 v[8:11], v1, s[28:29]
	s_add_u32 s28, s10, s6
	s_addc_u32 s29, s11, s7
	global_load_dwordx4 v[12:15], v1, s[28:29] offset:16
	global_load_dwordx4 v[16:19], v1, s[28:29]
	s_add_u32 s28, s12, s6
	s_addc_u32 s29, s13, s7
	global_load_dwordx4 v[20:23], v1, s[28:29] offset:16
	global_load_dwordx4 v[24:27], v1, s[28:29]
	s_add_u32 s28, s20, s6
	s_addc_u32 s29, s24, s7
	global_load_dwordx4 v[28:31], v1, s[28:29] offset:16
	global_load_dwordx4 v[32:35], v1, s[28:29]
	s_add_u32 s6, s6, 32
	s_addc_u32 s7, s7, 0
	s_cmpk_eq_i32 s6, 0x100
	s_waitcnt vmcnt(0)
	v_mov_b32_e32 v36, v8
	v_mov_b32_e32 v8, v10
	s_waitcnt vmcnt(5)
	v_mov_b32_e32 v10, v12
	s_waitcnt vmcnt(4)
	v_mov_b32_e32 v38, v16
	v_mov_b32_e32 v16, v18
	s_waitcnt vmcnt(2)
	v_mov_b32_e32 v37, v24
	v_mov_b32_e32 v24, v9
	v_mov_b32_e32 v9, v26
	s_waitcnt vmcnt(0)
	v_mov_b32_e32 v39, v32
	v_pk_fma_f32 v[2:3], v[36:37], v[38:39], v[2:3]
	v_mov_b32_e32 v32, v17
	v_pk_fma_f32 v[2:3], v[24:25], v[32:33], v[2:3]
	v_mov_b32_e32 v17, v34
	v_pk_fma_f32 v[2:3], v[8:9], v[16:17], v[2:3]
	v_mov_b32_e32 v26, v11
	v_mov_b32_e32 v34, v19
	v_pk_fma_f32 v[2:3], v[26:27], v[34:35], v[2:3]
	v_mov_b32_e32 v8, v4
	v_mov_b32_e32 v9, v20
	v_mov_b32_e32 v11, v28
	v_pk_fma_f32 v[2:3], v[8:9], v[10:11], v[2:3]
	v_mov_b32_e32 v20, v5
	v_mov_b32_e32 v28, v13
	v_pk_fma_f32 v[2:3], v[20:21], v[28:29], v[2:3]
	v_mov_b32_e32 v4, v6
	v_mov_b32_e32 v5, v22
	v_mov_b32_e32 v8, v14
	v_mov_b32_e32 v9, v30
	v_pk_fma_f32 v[2:3], v[4:5], v[8:9], v[2:3]
	v_mov_b32_e32 v22, v7
	v_mov_b32_e32 v30, v15
	v_pk_fma_f32 v[2:3], v[22:23], v[30:31], v[2:3]
	s_cbranch_scc0 .LBB0_1016
	v_cvt_f32_u32_e32 v4, s88
	s_mov_b32 s6, 0x3fb8aa3b
	s_lshl_b32 s7, s88, 9
	v_writelane_b32 v255, s7, 39
	v_mul_f32_e32 v4, 0xbe99999a, v4
	v_mul_f32_e32 v5, 0x3fb8aa3b, v4
	v_fma_f32 v6, v4, s6, -v5
	v_rndne_f32_e32 v7, v5
	v_fmac_f32_e32 v6, 0x32a5705f, v4
	v_sub_f32_e32 v5, v5, v7
	v_add_f32_e32 v5, v5, v6
	v_cvt_i32_f32_e32 v7, v7
	v_exp_f32_e32 v5, v5
	s_mov_b32 s7, 0xc2ce8ed0
	v_cmp_ngt_f32_e32 vcc, s7, v4
	s_mov_b32 s8, 0x42b17218
	v_ldexp_f32 v5, v5, v7
	v_cndmask_b32_e32 v5, 0, v5, vcc
	v_cmp_nlt_f32_e32 vcc, s8, v4
	v_mov_b32_e32 v9, 0x7f800000
	s_lshl_b32 s20, s88, 7
	v_cndmask_b32_e32 v4, v9, v5, vcc
	v_mov_b32_e32 v5, 0x3f4ccccd
	v_fmamk_f32 v4, v4, 0xbf19999a, v5
	v_sub_f32_e32 v5, 1.0, v4
	v_mul_f32_e32 v237, 0x41000000, v5
	v_mul_f32_e32 v5, 0x3fb8aa3b, v2
	v_rndne_f32_e32 v6, v5
	v_sub_f32_e32 v7, v5, v6
	v_fma_f32 v5, v2, s6, -v5
	v_fmac_f32_e32 v5, 0x32a5705f, v2
	v_add_f32_e32 v5, v7, v5
	v_exp_f32_e32 v5, v5
	v_cvt_i32_f32_e32 v6, v6
	v_cmp_ngt_f32_e32 vcc, s7, v2
	s_add_u32 s13, s4, 0x21200000
	s_addc_u32 s94, s5, 0
	v_ldexp_f32 v5, v5, v6
	v_mul_f32_e32 v6, 0x3fb8aa3b, v3
	v_rndne_f32_e32 v7, v6
	v_sub_f32_e32 v8, v6, v7
	v_fma_f32 v6, v3, s6, -v6
	v_fmac_f32_e32 v6, 0x32a5705f, v3
	v_add_f32_e32 v6, v8, v6
	v_exp_f32_e32 v6, v6
	v_cvt_i32_f32_e32 v7, v7
	v_cndmask_b32_e32 v5, 0, v5, vcc
	v_cmp_nlt_f32_e32 vcc, s8, v2
	s_add_u32 s95, s4, 0x1d200000
	v_bfe_u32 v241, v0, 4, 2
	v_cndmask_b32_e32 v2, v9, v5, vcc
	v_ldexp_f32 v5, v6, v7
	v_cmp_ngt_f32_e32 vcc, s7, v3
	v_add_u32_e32 v238, s67, v0
	s_addc_u32 s96, s5, 0
	v_cndmask_b32_e32 v5, 0, v5, vcc
	v_cmp_nlt_f32_e32 vcc, s8, v3
	v_and_b32_e32 v240, 31, v0
	v_and_b32_e32 v7, 15, v0
	v_cndmask_b32_e32 v3, v9, v5, vcc
	v_sub_f32_e32 v2, v2, v3
	v_and_b32_e32 v3, 63, v0
	v_add_f32_e32 v239, v4, v2
	v_bfe_u32 v5, v0, 5, 1
	v_bitop3_b32 v2, v241, v0, 15 bitop3:0x78
	v_bfe_u32 v242, v0, 2, 4
	v_lshlrev_b32_e32 v6, 3, v0
	v_lshlrev_b32_e32 v8, 1, v0
	v_lshlrev_b32_e32 v10, 4, v0
	v_cmp_gt_u32_e64 s[40:41], 32, v3
	v_lshrrev_b32_e32 v3, 1, v0
	v_and_b32_e32 v0, 3, v0
	s_add_u32 s6, s4, 0x18000
	v_and_b32_e32 v6, 24, v6
	v_and_b32_e32 v8, 32, v8
	v_lshlrev_b32_e32 v0, 4, v0
	v_writelane_b32 v255, s6, 41
	s_addc_u32 s6, s5, 0
	v_bitop3_b32 v4, v241, v7, 4 bitop3:0x36
	v_add3_u32 v8, 0, v8, v6
	v_lshlrev_b32_e32 v9, 8, v5
	v_and_b32_e32 v11, 0xc0, v10
	v_lshl_add_u64 v[14:15], s[4:5], 0, v[0:1]
	s_mov_b64 s[4:5], 0x212d1000
	s_getreg_b32 s97, hwreg(HW_REG_XCC_ID, 0, 4)
	v_lshlrev_b32_e32 v2, 3, v2
	v_lshlrev_b32_e32 v4, 3, v4
	v_add3_u32 v243, v8, v9, v11
	v_and_b32_e32 v246, 0xf0, v10
	v_lshlrev_b32_e32 v8, 3, v5
	v_and_b32_e32 v10, 4, v3
	v_bitop3_b32 v12, v3, 4, v3 bitop3:0xc
	v_lshl_add_u64 v[200:201], v[14:15], 0, s[4:5]
	s_mov_b64 s[4:5], 0x241f1000
	s_mov_b32 s67, 0
	v_cmp_eq_u32_e64 s[38:39], 0, v238
	v_writelane_b32 v255, s6, 42
	v_add_u32_e32 v244, 0xc000, v243
	v_lshlrev_b32_e32 v245, 4, v5
	v_lshlrev_b32_e32 v247, 8, v240
	v_lshlrev_b32_e32 v248, 11, v5
	v_lshlrev_b32_e32 v198, 3, v7
	v_mov_b32_e32 v199, v1
	v_lshlrev_b32_e32 v249, 9, v241
	v_cmp_gt_u32_e64 s[42:43], 8, v7
	v_lshl_add_u64 v[202:203], v[14:15], 0, s[4:5]
	v_lshlrev_b32_e32 v0, 1, v2
	v_lshlrev_b32_e32 v204, 1, v4
	v_lshlrev_b32_e32 v206, 1, v6
	v_lshlrev_b32_e32 v208, 1, v8
	s_lshl_b64 s[84:85], s[20:21], 2
	v_lshlrev_b32_e32 v210, 2, v10
	v_lshlrev_b32_e32 v212, 2, v12
	s_mov_b32 s73, s97
	s_branch .LBB0_1019

.LBB0_1026:
	s_or_b64 exec, exec, s[4:5]
	v_mov_b32_e32 v2, s2
	s_waitcnt lgkmcnt(0)
	s_barrier
	ds_read_b32 v2, v2
	s_mov_b64 s[4:5], -1
	s_waitcnt lgkmcnt(0)
	s_barrier
	v_readfirstlane_b32 s7, v2
	s_cmpk_gt_i32 s7, 0x7f
	s_cbranch_scc1 .LBB0_1021
	s_ashr_i32 s6, s7, 5
	s_add_i32 s8, s6, s28
	s_ashr_i32 s4, s8, 3
	s_ashr_i32 s5, s4, 31
	s_lshl_b64 s[90:91], s[4:5], 12
	s_lshl_b32 s5, s7, 7
	s_and_b32 s5, s5, 0xf80
	s_or_b32 s90, s90, s5
	s_mul_i32 s5, s91, 0x3400
	s_mul_hi_u32 s7, s90, 0x3400
	s_add_i32 s7, s7, s5
	s_mul_i32 s5, s90, 0x3400
	s_add_u32 s5, s13, s5
	s_addc_u32 s7, s94, s7
	s_lshl_b32 s8, s8, 7
	s_and_b32 s29, s8, 0x380
	s_lshl_b32 s10, s29, 1
	s_add_u32 s8, s5, s10
	s_addc_u32 s9, s7, 0
	s_mul_i32 s11, s4, 0x3400000
	s_mul_hi_i32 s7, s4, 0x3400000
	s_add_u32 s4, s13, s11
	s_addc_u32 s5, s94, s7
	s_add_u32 s4, s4, s10
	v_readfirstlane_b32 s10, v238
	s_addc_u32 s5, s5, 0
	s_ashr_i32 s20, s10, 6
	v_lshl_or_b32 v6, s20, 3, v241
	v_mov_b64_e32 v[2:3], s[4:5]
	v_mad_i64_i32 v[4:5], s[44:45], v6, s83, v[2:3]
	v_lshl_add_u64 v[50:51], v[4:5], 0, v[0:1]
	v_or_b32_e32 v4, 4, v6
	s_and_b32 s24, s20, 1
	v_mad_i64_i32 v[2:3], s[44:45], v4, s83, v[2:3]
	v_mov_b32_e32 v205, v1
	s_ashr_i32 s25, s10, 7
	v_lshl_add_u64 v[54:55], v[2:3], 0, v[204:205]
	s_lshl_b32 vcc_lo, s24, 7
	v_xor_b32_e32 v50, vcc_lo, v50
	v_xor_b32_e32 v54, vcc_lo, v54
	v_lshl_or_b32 v2, s24, 5, v242
	s_mov_b32 s72, s88
	v_mul_u32_u24_e32 v2, 0x1a00, v2
	s_lshl_b32 s88, s25, 5
	v_lshlrev_b32_e32 v52, 1, v2
	v_mov_b32_e32 v53, v1
	s_ashr_i32 s89, s88, 31
	s_and_b32 s71, s10, 0x3fffffc0
	v_lshl_add_u64 v[2:3], s[4:5], 0, v[52:53]
	s_lshl_b64 s[4:5], s[88:89], 1
	s_lshl_b32 s89, s20, 11
	s_cmp_lg_u32 0, -1
	s_cselect_b32 s10, 0, 0
	s_lshl_b32 s25, s25, 12
	v_lshl_add_u64 v[2:3], v[2:3], 0, s[4:5]
	v_mov_b32_e32 v207, v1
	s_add_i32 s89, s89, s10
	s_add_i32 s10, s10, s25
	s_lshl_b32 s20, s24, 11
	s_load_dwordx2 s[92:93], s[60:61], 0xc0
	v_lshl_add_u64 v[214:215], v[50:51], 0, s[30:31]
	v_lshl_add_u64 v[56:57], v[2:3], 0, v[206:207]
	s_add_i32 s70, s10, s20
	s_mov_b32 s10, m0
	s_mov_b32 m0, s89
	s_nop 0
	global_load_lds_dwordx4 v[214:215], off
	s_mov_b32 m0, s10
	s_add_i32 vcc_lo, s89, 0x400
	v_lshl_add_u64 v[216:217], v[54:55], 0, s[30:31]
	v_lshl_add_u64 v[2:3], v[56:57], 0, s[14:15]
	s_mov_b32 s10, m0
	s_mov_b32 m0, vcc_lo
	s_nop 0
	global_load_lds_dwordx4 v[216:217], off
	s_mov_b32 m0, s10
	s_mov_b64 s[44:45], 0x35000
	s_add_i32 s70, s70, 0xc000
	s_mov_b32 s10, m0
	s_mov_b32 m0, s70
	s_nop 0
	global_load_lds_dwordx4 v[2:3], off
	s_mov_b32 m0, s10
	v_lshl_add_u64 v[2:3], v[56:57], 0, s[44:45]
	s_add_i32 s10, s70, 0x400
	s_mov_b32 s44, m0
	s_mov_b32 m0, s10
	s_nop 0
	global_load_lds_dwordx4 v[2:3], off
	s_mov_b32 m0, s44
	v_lshl_add_u64 v[2:3], v[50:51], 0, s[34:35]
	s_add_i32 s10, s89, 0x4000
	s_mov_b32 s44, m0
	s_mov_b32 m0, s10
	s_nop 0
	global_load_lds_dwordx4 v[2:3], off
	s_mov_b32 m0, s44
	v_lshl_add_u64 v[2:3], v[54:55], 0, s[34:35]
	s_add_i32 s10, s89, 0x4400
	s_mov_b32 s44, m0
	s_mov_b32 m0, s10
	s_nop 0
	global_load_lds_dwordx4 v[2:3], off
	s_mov_b32 m0, s44
	v_or_b32_e32 v4, s88, v240
	v_mov_b64_e32 v[2:3], s[8:9]
	s_lshl_b32 s20, s24, 7
	v_mad_i64_i32 v[2:3], s[8:9], v4, s83, v[2:3]
	v_lshl_add_u64 v[2:3], v[2:3], 0, s[20:21]
	v_mov_b32_e32 v209, v1
	v_lshl_add_u64 v[2:3], v[2:3], 0, v[208:209]
	global_load_dwordx4 v[158:161], v[2:3], off nt
	global_load_dwordx4 v[154:157], v[2:3], off offset:32 nt
	global_load_dwordx4 v[146:149], v[2:3], off offset:64 nt
	global_load_dwordx4 v[142:145], v[2:3], off offset:96 nt
	v_lshl_add_u64 v[2:3], v[50:51], 0, s[36:37]
	v_or_b32_e32 v6, s20, v245
	s_add_i32 s8, s89, 0x8000
	s_mov_b32 s10, m0
	s_mov_b32 m0, s8
	s_nop 0
	global_load_lds_dwordx4 v[2:3], off
	s_mov_b32 m0, s10
	v_lshl_add_u64 v[4:5], v[54:55], 0, s[36:37]
	v_bitop3_b32 v209, v6, v247, v246 bitop3:0xde
	s_add_i32 s9, s89, 0x8400
	s_mov_b32 s8, m0
	s_mov_b32 m0, s9
	s_nop 0
	global_load_lds_dwordx4 v[4:5], off
	s_mov_b32 m0, s8
	v_add_u32_e32 v211, 0, v209
	s_waitcnt vmcnt(6) lgkmcnt(0)
	s_barrier
	ds_read_b128 v[2:5], v211
	ds_read_b128 v[6:9], v211 offset:8192
	v_bitop3_b32 v10, s20, v246, v245 bitop3:0x36
	v_bitop3_b32 v213, v10, 32, v247 bitop3:0x36
	v_add_u32_e32 v250, 0, v213
	v_bitop3_b32 v251, v10, 64, v247 bitop3:0x36
	v_add_u32_e32 v252, 0, v251
	s_movk_i32 s20, 0x60
	v_bitop3_b32 v235, v10, s20, v247 bitop3:0x36
	v_add_u32_e32 v227, 0, v235
	s_mov_b32 s44, 0
	s_mov_b32 s45, s44
	s_mov_b32 s46, s44
	s_mov_b32 s47, s44
	s_mov_b32 s48, s44
	s_mov_b32 s49, s44
	s_mov_b32 s50, s44
	s_mov_b32 s51, s44
	s_mov_b32 s52, s44
	s_waitcnt vmcnt(3) lgkmcnt(0)
	v_mfma_f32_32x32x16_bf16 v[18:33], v[2:5], v[158:161], 0
	s_mov_b32 s53, s44
	s_mov_b32 s54, s44
	s_mov_b32 s55, s44
	s_mov_b32 s56, s44
	s_mov_b32 s57, s44
	s_mov_b32 s58, s44
	s_mov_b32 s59, s44
	v_mfma_f32_32x32x16_bf16 v[34:49], v[6:9], v[158:161], 0
	ds_read_b128 v[2:5], v250
	ds_read_b128 v[6:9], v250 offset:8192
	ds_read_b128 v[58:61], v227 offset:8192
	s_lshl_b32 s6, s6, 7
	s_add_i32 s6, s12, s6
	s_lshl_b32 s6, s6, 1
	s_and_b32 s6, s6, 0x700
	s_or_b32 s6, s11, s6
	s_waitcnt vmcnt(2) lgkmcnt(2)
	v_mfma_f32_32x32x16_bf16 v[18:33], v[2:5], v[154:157], v[18:33]
	ds_read_b128 v[2:5], v252
	v_lshl_add_u64 v[218:219], v[54:55], 0, s[16:17]
	v_lshl_add_u64 v[220:221], v[50:51], 0, s[16:17]
	s_mov_b32 s8, -1
	s_movk_i32 s10, 0x4000
	s_mov_b32 s9, 0x8000
	v_mov_b32_e32 v234, 0
	s_waitcnt lgkmcnt(2)
	v_mfma_f32_32x32x16_bf16 v[34:49], v[6:9], v[154:157], v[34:49]
	ds_read_b128 v[6:9], v252 offset:8192
	s_waitcnt vmcnt(1) lgkmcnt(1)
	v_mfma_f32_32x32x16_bf16 v[18:33], v[2:5], v[146:149], v[18:33]
	ds_read_b128 v[2:5], v227
	s_waitcnt vmcnt(0) lgkmcnt(0)
	s_barrier
	s_waitcnt lgkmcnt(1)
	v_mfma_f32_32x32x16_bf16 v[34:49], v[6:9], v[146:149], v[34:49]
	s_waitcnt vmcnt(0) lgkmcnt(0)
	v_mfma_f32_32x32x16_bf16 v[18:33], v[2:5], v[142:145], v[18:33]
	v_mov_b64_e32 v[2:3], s[44:45]
	v_mov_b64_e32 v[4:5], s[46:47]
	v_mov_b64_e32 v[6:7], s[48:49]
	v_mov_b64_e32 v[8:9], s[50:51]
	v_mov_b64_e32 v[10:11], s[52:53]
	v_mov_b64_e32 v[12:13], s[54:55]
	v_mov_b64_e32 v[14:15], s[56:57]
	v_mfma_f32_32x32x16_bf16 v[34:49], v[58:61], v[142:145], v[34:49]
	s_nop 3
	v_max_f32_e32 v58, v19, v19
	v_max_f32_e32 v59, v18, v18
	v_max_f32_e32 v58, v59, v58
	v_mov_b64_e32 v[16:17], s[58:59]
	s_mov_b64 s[46:47], 0xd1000
	s_nop 2
	v_max3_f32 v59, v20, v21, v35
	v_max3_f32 v58, v58, v34, v36
	v_max3_f32 v58, v58, v37, v22
	v_max3_f32 v59, v59, v24, v25
	v_max3_f32 v58, v58, v23, v38
	v_max3_f32 v59, v59, v40, v41
	v_max3_f32 v58, v58, v39, v26
	v_max3_f32 v59, v59, v28, v29
	v_max3_f32 v58, v58, v27, v42
	v_max3_f32 v59, v59, v44, v45
	v_max3_f32 v58, v58, v43, v30
	v_max3_f32 v59, v59, v32, v33
	v_max3_f32 v58, v58, v31, v46
	v_max3_f32 v59, v59, v48, v49
	v_max3_f32 v58, v58, v47, v59
	v_mov_b32_e32 v59, v58
	s_nop 1
	v_permlane32_swap_b32_e32 v58, v59
	v_max_f32_e32 v59, v59, v59
	v_max_f32_e32 v58, v58, v58
	v_max_f32_e32 v207, v58, v59
	v_sub_f32_e32 v18, v18, v207
	v_exp_f32_e32 v82, v18
	v_sub_f32_e32 v18, v34, v207
	v_exp_f32_e32 v66, v18
	v_sub_f32_e32 v18, v19, v207
	v_exp_f32_e32 v83, v18
	v_sub_f32_e32 v18, v35, v207
	v_exp_f32_e32 v67, v18
	v_sub_f32_e32 v18, v20, v207
	v_exp_f32_e32 v84, v18
	v_sub_f32_e32 v18, v36, v207
	v_exp_f32_e32 v68, v18
	v_sub_f32_e32 v18, v21, v207
	v_exp_f32_e32 v85, v18
	v_sub_f32_e32 v18, v37, v207
	v_exp_f32_e32 v69, v18
	v_sub_f32_e32 v18, v22, v207
	v_exp_f32_e32 v86, v18
	v_sub_f32_e32 v18, v38, v207
	v_exp_f32_e32 v70, v18
	v_sub_f32_e32 v18, v23, v207
	v_exp_f32_e32 v87, v18
	v_sub_f32_e32 v18, v39, v207
	v_exp_f32_e32 v71, v18
	v_sub_f32_e32 v18, v24, v207
	v_exp_f32_e32 v88, v18
	v_sub_f32_e32 v18, v40, v207
	v_exp_f32_e32 v72, v18
	v_sub_f32_e32 v18, v25, v207
	v_exp_f32_e32 v89, v18
	v_sub_f32_e32 v18, v41, v207
	v_exp_f32_e32 v73, v18
	v_sub_f32_e32 v18, v26, v207
	v_exp_f32_e32 v90, v18
	v_sub_f32_e32 v18, v42, v207
	v_exp_f32_e32 v74, v18
	v_sub_f32_e32 v18, v27, v207
	v_exp_f32_e32 v91, v18
	v_sub_f32_e32 v18, v43, v207
	v_exp_f32_e32 v75, v18
	v_sub_f32_e32 v18, v28, v207
	v_exp_f32_e32 v92, v18
	v_sub_f32_e32 v18, v44, v207
	v_exp_f32_e32 v76, v18
	v_sub_f32_e32 v18, v29, v207
	v_exp_f32_e32 v93, v18
	v_sub_f32_e32 v18, v45, v207
	v_exp_f32_e32 v77, v18
	v_sub_f32_e32 v18, v30, v207
	v_exp_f32_e32 v94, v18
	v_sub_f32_e32 v18, v46, v207
	v_exp_f32_e32 v78, v18
	v_sub_f32_e32 v18, v31, v207
	v_exp_f32_e32 v95, v18
	v_sub_f32_e32 v18, v47, v207
	v_exp_f32_e32 v79, v18
	v_sub_f32_e32 v18, v32, v207
	v_exp_f32_e32 v96, v18
	v_sub_f32_e32 v18, v48, v207
	v_exp_f32_e32 v80, v18
	v_sub_f32_e32 v18, v33, v207
	v_exp_f32_e32 v97, v18
	v_sub_f32_e32 v18, v49, v207
	v_exp_f32_e32 v81, v18
	v_lshl_add_u64 v[18:19], v[50:51], 0, s[18:19]
	s_mov_b32 s20, m0
	s_mov_b32 m0, s89
	s_nop 0
	global_load_lds_dwordx4 v[18:19], off
	s_mov_b32 m0, s20
	v_lshl_add_u64 v[18:19], v[54:55], 0, s[18:19]
	s_mov_b32 s20, m0
	s_mov_b32 m0, vcc_lo
	s_nop 0
	global_load_lds_dwordx4 v[18:19], off
	s_mov_b32 m0, s20
	v_lshl_add_u64 v[18:19], v[56:57], 0, s[46:47]
	s_add_i32 s20, s70, 0x4000
	s_mov_b32 s45, m0
	s_mov_b32 m0, s20
	s_nop 0
	global_load_lds_dwordx4 v[18:19], off
	s_mov_b32 m0, s45
	s_mov_b64 s[46:47], 0x105000
	v_lshl_add_u64 v[18:19], v[56:57], 0, s[46:47]
	s_add_i32 s20, s70, 0x4400
	s_mov_b32 s45, m0
	s_mov_b32 m0, s20
	s_nop 0
	global_load_lds_dwordx4 v[18:19], off
	s_mov_b32 m0, s45
	ds_read_b128 v[102:105], v211 offset:16384
	ds_read_b128 v[98:101], v211 offset:24576
	ds_read_b128 v[182:185], v250 offset:16384
	ds_read_b128 v[178:181], v250 offset:24576
	ds_read_b128 v[174:177], v252 offset:16384
	ds_read_b128 v[170:173], v252 offset:24576
	ds_read_b128 v[166:169], v227 offset:16384
	ds_read_b128 v[162:165], v227 offset:24576
	s_lshl_b32 s20, s71, 2
	s_add_i32 s20, s20, 0
	s_add_i32 s20, s20, 0x18000
	s_add_u32 s4, s6, s4
	s_waitcnt vmcnt(4) lgkmcnt(0)
	s_barrier
	s_addc_u32 s5, s7, s5
	v_lshl_add_u64 v[222:223], s[4:5], 0, v[52:53]
	v_mov_b64_e32 v[64:65], v[16:17]
	v_mov_b64_e32 v[48:49], v[16:17]
	v_mov_b64_e32 v[32:33], v[16:17]
	v_lshl_add_u32 v205, v240, 2, s20
	v_lshl_add_u64 v[224:225], v[200:201], 0, v[222:223]
	v_mov_b64_e32 v[62:63], v[14:15]
	v_mov_b64_e32 v[60:61], v[12:13]
	v_mov_b64_e32 v[58:59], v[10:11]
	v_mov_b64_e32 v[56:57], v[8:9]
	v_mov_b64_e32 v[54:55], v[6:7]
	v_mov_b64_e32 v[52:53], v[4:5]
	v_mov_b64_e32 v[50:51], v[2:3]
	v_mov_b64_e32 v[46:47], v[14:15]
	v_mov_b64_e32 v[44:45], v[12:13]
	v_mov_b64_e32 v[42:43], v[10:11]
	v_mov_b64_e32 v[40:41], v[8:9]
	v_mov_b64_e32 v[38:39], v[6:7]
	v_mov_b64_e32 v[36:37], v[4:5]
	v_mov_b64_e32 v[34:35], v[2:3]
	v_mov_b64_e32 v[30:31], v[14:15]
	v_mov_b64_e32 v[28:29], v[12:13]
	v_mov_b64_e32 v[26:27], v[10:11]
	v_mov_b64_e32 v[24:25], v[8:9]
	v_mov_b64_e32 v[22:23], v[6:7]
	v_mov_b64_e32 v[20:21], v[4:5]
	v_mov_b64_e32 v[18:19], v[2:3]
	v_mbcnt_lo_u32_b32 v230, -1, 0
	v_mbcnt_hi_u32_b32 v230, -1, v230
	v_and_b32_e32 v230, 32, v230
	v_lshl_add_u32 v230, v230, 2, v205
	ds_write_b32 v230, v237 offset:2048
	ds_write_b32 v230, v238 offset:4096
	ds_write_b32 v230, v239 offset:6144
	ds_write_b32 v230, v240 offset:8192
	ds_write_b32 v230, v241 offset:10240
	ds_write_b32 v230, v242 offset:12288
	ds_write_b32 v230, v244 offset:14336
	ds_write_b32 v230, v246 offset:16384
	s_waitcnt lgkmcnt(0)
	ds_write_b32 v230, v247 offset:18432
	ds_write_b32 v230, v248 offset:20480
	ds_write_b32 v230, v249 offset:22528
	ds_write_b32 v230, v250 offset:24576
	ds_write_b32 v230, v228 offset:26624
	ds_write_b32 v230, v229 offset:28672
	ds_write_b32 v230, v231 offset:30720
	s_waitcnt lgkmcnt(0)
	v_mov_b32_e32 v228, v243
	v_mov_b32_e32 v229, v245
	v_mov_b32_e32 v231, v251
	v_sub_f32_e32 v236, 0, v207
	v_sub_f32_e32 v237, 0, v207
	v_sub_f32_e32 v238, 0, v207
	v_sub_f32_e32 v239, 0, v207
	v_sub_f32_e32 v240, 0, v207
	v_sub_f32_e32 v241, 0, v207
	v_sub_f32_e32 v242, 0, v207
	v_sub_f32_e32 v243, 0, v207
	v_sub_f32_e32 v244, 0, v207
	v_sub_f32_e32 v245, 0, v207
	v_sub_f32_e32 v246, 0, v207
	v_sub_f32_e32 v247, 0, v207
	v_sub_f32_e32 v248, 0, v207
	v_sub_f32_e32 v249, 0, v207
	v_sub_f32_e32 v250, 0, v207
	v_sub_f32_e32 v251, 0, v207
